# speedup vs baseline: 1.0143x; 1.0143x over previous
.LBB5_150:
	s_lshl_b32 s10, s33, 11
	s_add_u32 s16, s34, s10
	s_addc_u32 s17, s35, 0
	v_mov_b32_e32 v83, 0
	v_lshl_add_u64 v[0:1], s[16:17], 0, v[82:83]
	s_mov_b64 s[16:17], 0x144000
	v_cmp_gt_u32_e64 s[10:11], 31, v128
	v_cmp_lt_u32_e64 s[12:13], 30, v128
	v_lshl_add_u64 v[0:1], v[0:1], 0, s[16:17]
	v_mov_b64_e32 v[2:3], 0
	s_mov_b32 s24, 0x400001
	s_mov_b64 s[16:17], 0xffffffff
	s_sleep 4
	s_branch .LBB5_152
